# P5 epilogue constant loads: one base VGPR + ds_read immediate offsets (6 fewer VALU), later code kept at the same addresses
# baseline (speedup 1.0000x reference)
; #define PG8_LAS __attribute__((address_space(3)))
;     __device__ __forceinline__ void operator()(const i32x4 (&acc)[2][2][4][2], const Unit& u, int wr, int wc, int fr, int fq, PG8_LAS unsigned* scr) const {
;         const int j = u.pn & 7;
;         const int row0 = u.pm * BM + wr * 64 + fr, c0 = j * 128 + wc * 32 + 8 * fq, cl = wc * 32 + 8 * fq;
;         f32x4 bgv[2], buv[2], csg[2], csu[2];
;         constexpr float C2 = 1.702f * 1.44269504f;
; #pragma unroll
;         for (int n = 0; n < 2; ++n) { bgv[n] = *(const PG8_LAS f32x4*)(scr + 512 + cl + 4 * n) * C2; buv[n] = *(const PG8_LAS f32x4*)(scr + 512 + 128 + cl + 4 * n);
;             csg[n] = *(const PG8_LAS f32x4*)(scr + 256 + cl + 4 * n) * (C2 / 127.0f); csu[n] = *(const PG8_LAS f32x4*)(scr + 256 + 128 + cl + 4 * n) * (1.0f / 127.0f); }
; #pragma unroll
;         for (int ai = 0; ai < 2; ++ai)
; #pragma unroll
;             for (int mp = 0; mp < 4; mp += 2) { unsigned wp[2][2];
; #pragma unroll
;                 for (int hm = 0; hm < 2; ++hm) { const int m = mp + hm; const int r = ai * HALF + wr * 64 + m * 16 + fr; const float rs = __uint_as_float(scr[r]); float o[8];
; #pragma unroll
;                     for (int n = 0; n < 2; ++n) { const f32x4 sgr = csg[n] * rs, sur = csu[n] * rs;
; #pragma unroll
;                         for (int q = 0; q < 4; ++q) { const float h = fminf(__builtin_fmaf((float)acc[ai][0][m][n][q], sgr[q], bgv[n][q]), 7.0f * C2), up = fminf(fmaxf(__builtin_fmaf((float)acc[ai][1][m][n][q], sur[q], buv[n][q]), -7.0f), 7.0f);
;                             const float sg = __builtin_amdgcn_rcpf(1.0f + __builtin_amdgcn_exp2f(-h)); o[4 * n + q] = __builtin_fmaf(up, ACT_SC / C2, ACT_SC / C2) * (h * sg); } }
;                     int w0 = __builtin_amdgcn_cvt_pk_fp8_f32(o[0], o[1], 0, false); w0 = __builtin_amdgcn_cvt_pk_fp8_f32(o[2], o[3], w0, true);
;                     int w1 = __builtin_amdgcn_cvt_pk_fp8_f32(o[4], o[5], 0, false); w1 = __builtin_amdgcn_cvt_pk_fp8_f32(o[6], o[7], w1, true);
;                     wp[hm][0] = (unsigned)w0; wp[hm][1] = (unsigned)w1; }
.LBB0_807:
	v_ashrrev_i32_e32 v185, 2, v168
	v_and_b32_e32 v185, 0xffffffc0, v185
	v_bfe_u32 v201, v168, 4, 2
	v_lshrrev_b32_e32 v208, 1, v168
	v_and_b32_e32 v208, 0x60, v208
	v_lshl_or_b32 v208, v201, 3, v208
	s_lshl_b32 s10, s39, 7
	s_and_b32 s10, s10, 0x380
	v_and_b32_e32 v201, 1, v201
	v_lshlrev_b32_e32 v207, 3, v201
	v_add_u32_e32 v206, s10, v208
	v_sub_u32_e32 v206, v206, v207
	v_mov_b32_e32 v207, 0
	v_lshlrev_b32_e32 v201, 4, v201
	v_lshlrev_b32_e32 v208, 2, v208
	v_readlane_b32 s10, v255, 5
	v_and_b32_e32 v160, 15, v168
	v_lshl_add_u32 v161, v185, 2, 0
	v_lshl_add_u32 v161, v160, 2, v161
	v_add_u32_e32 v161, s10, v161
	ds_read2_b32 v[152:153], v161 offset0:0 offset1:16
	ds_read2_b32 v[154:155], v161 offset0:32 offset1:48
	ds_read2_b32 v[156:157], v161 offset0:128 offset1:144
	ds_read2_b32 v[158:159], v161 offset0:160 offset1:176
	v_lshl_add_u32 v185, s40, 8, v185
	v_or_b32_e32 v185, v185, v160
	v_add_u32_e32 v185, v185, v201
	v_lshl_add_u32 v207, v185, 10, v206
	s_mov_b32 s100, 0x405083aa
	s_mov_b32 s101, 0x405083aa
	v_add_u32_e32 v160, 0x20d00, v208
	ds_read_b128 v[136:139], v160 offset:1024
	ds_read_b128 v[140:143], v160 offset:1536
	ds_read_b128 v[144:147], v160
	ds_read_b128 v[148:151], v160 offset:512
	s_waitcnt lgkmcnt(0)
	v_mul_f32_e32 v136, 0x401d265f, v136
	v_mul_f32_e32 v137, 0x401d265f, v137
	v_mul_f32_e32 v138, 0x401d265f, v138
	v_mul_f32_e32 v139, 0x401d265f, v139
	v_mul_f32_e32 v144, 0x3c9e6325, v144
	v_mul_f32_e32 v145, 0x3c9e6325, v145
	v_mul_f32_e32 v146, 0x3c9e6325, v146
	v_mul_f32_e32 v147, 0x3c9e6325, v147
	v_mul_f32_e32 v148, 0x3c010204, v148
	v_mul_f32_e32 v149, 0x3c010204, v149
	v_mul_f32_e32 v150, 0x3c010204, v150
	v_mul_f32_e32 v151, 0x3c010204, v151
	v_cvt_f32_i32_e32 v128, v128
	v_cvt_f32_i32_e32 v129, v129
	v_cvt_f32_i32_e32 v130, v130
	v_cvt_f32_i32_e32 v131, v131
	v_cvt_f32_i32_e32 v132, v132
	v_cvt_f32_i32_e32 v133, v133
	v_cvt_f32_i32_e32 v134, v134
	v_cvt_f32_i32_e32 v135, v135
	v_pk_mul_f32 v[160:161], v[144:145], v[152:153] op_sel_hi:[1,0]
	v_pk_mul_f32 v[162:163], v[146:147], v[152:153] op_sel_hi:[1,0]
	v_pk_fma_f32 v[128:129], v[128:129], v[160:161], v[136:137]
	v_pk_fma_f32 v[130:131], v[130:131], v[162:163], v[138:139]
	v_pk_mul_f32 v[160:161], v[148:149], v[152:153] op_sel_hi:[1,0]
	v_pk_mul_f32 v[162:163], v[150:151], v[152:153] op_sel_hi:[1,0]
	v_min_f32_e32 v128, 0x41898193, v128
	v_min_f32_e32 v129, 0x41898193, v129
	v_min_f32_e32 v130, 0x41898193, v130
	v_min_f32_e32 v131, 0x41898193, v131
	v_pk_fma_f32 v[132:133], v[132:133], v[160:161], v[140:141]
	v_pk_fma_f32 v[134:135], v[134:135], v[162:163], v[142:143]
	v_exp_f32_e64 v160, -v128
	v_exp_f32_e64 v161, -v129
	v_exp_f32_e64 v162, -v130
	v_exp_f32_e64 v163, -v131
	v_med3_f32 v132, v132, s8, v199
	v_med3_f32 v133, v133, s8, v199
	v_med3_f32 v134, v134, s8, v199
	v_med3_f32 v135, v135, s8, v199
	v_pk_add_f32 v[160:161], v[160:161], 1.0 op_sel_hi:[1,0]
	v_pk_add_f32 v[162:163], v[162:163], 1.0 op_sel_hi:[1,0]
	v_rcp_f32_e32 v160, v160
	v_rcp_f32_e32 v161, v161
	v_rcp_f32_e32 v162, v162
	v_rcp_f32_e32 v163, v163
	v_pk_fma_f32 v[132:133], v[132:133], s[100:101], s[100:101]
	v_pk_fma_f32 v[134:135], v[134:135], s[100:101], s[100:101]
	v_pk_mul_f32 v[128:129], v[128:129], v[160:161]
	v_pk_mul_f32 v[130:131], v[130:131], v[162:163]
	v_pk_mul_f32 v[128:129], v[132:133], v[128:129]
	v_pk_mul_f32 v[130:131], v[134:135], v[130:131]
	v_cvt_pk_fp8_f32 v128, v128, v129
	v_cvt_pk_fp8_f32 v128, v130, v131 op_sel:[0,0,1]
	s_and_b64 vcc, exec, s[62:63]
	s_cbranch_vccz .Lp5_epi_nobar
	s_barrier
.Lp5_epi_nobar:
	v_cvt_f32_i32_e32 v112, v112
	v_cvt_f32_i32_e32 v113, v113
	v_cvt_f32_i32_e32 v114, v114
	v_cvt_f32_i32_e32 v115, v115
	v_cvt_f32_i32_e32 v116, v116
	v_cvt_f32_i32_e32 v117, v117
	v_cvt_f32_i32_e32 v118, v118
	v_cvt_f32_i32_e32 v119, v119
	v_pk_mul_f32 v[202:203], v[144:145], v[152:153] op_sel:[0,1] op_sel_hi:[1,1]
	v_pk_mul_f32 v[204:205], v[146:147], v[152:153] op_sel:[0,1] op_sel_hi:[1,1]
	v_pk_fma_f32 v[112:113], v[112:113], v[202:203], v[136:137]
	v_pk_fma_f32 v[114:115], v[114:115], v[204:205], v[138:139]
	v_pk_mul_f32 v[202:203], v[148:149], v[152:153] op_sel:[0,1] op_sel_hi:[1,1]
	v_pk_mul_f32 v[204:205], v[150:151], v[152:153] op_sel:[0,1] op_sel_hi:[1,1]
	v_min_f32_e32 v112, 0x41898193, v112
	v_min_f32_e32 v113, 0x41898193, v113
	v_min_f32_e32 v114, 0x41898193, v114
	v_min_f32_e32 v115, 0x41898193, v115
	v_pk_fma_f32 v[116:117], v[116:117], v[202:203], v[140:141]
	v_pk_fma_f32 v[118:119], v[118:119], v[204:205], v[142:143]
	v_exp_f32_e64 v202, -v112
	v_exp_f32_e64 v203, -v113
	v_exp_f32_e64 v204, -v114
	v_exp_f32_e64 v205, -v115
	v_med3_f32 v116, v116, s8, v199
	v_med3_f32 v117, v117, s8, v199
	v_med3_f32 v118, v118, s8, v199
	v_med3_f32 v119, v119, s8, v199
	v_pk_add_f32 v[202:203], v[202:203], 1.0 op_sel_hi:[1,0]
	v_pk_add_f32 v[204:205], v[204:205], 1.0 op_sel_hi:[1,0]
	v_rcp_f32_e32 v202, v202
	v_rcp_f32_e32 v203, v203
	v_rcp_f32_e32 v204, v204
	v_rcp_f32_e32 v205, v205
	v_pk_fma_f32 v[116:117], v[116:117], s[100:101], s[100:101]
	v_pk_fma_f32 v[118:119], v[118:119], s[100:101], s[100:101]
	v_pk_mul_f32 v[112:113], v[112:113], v[202:203]
	v_pk_mul_f32 v[114:115], v[114:115], v[204:205]
	v_pk_mul_f32 v[112:113], v[116:117], v[112:113]
	v_pk_mul_f32 v[114:115], v[118:119], v[114:115]
	v_cvt_pk_fp8_f32 v130, v112, v113
	v_cvt_pk_fp8_f32 v130, v114, v115 op_sel:[0,0,1]
	v_cvt_f32_i32_e32 v96, v96
	v_cvt_f32_i32_e32 v97, v97
	v_cvt_f32_i32_e32 v98, v98
	v_cvt_f32_i32_e32 v99, v99
	v_cvt_f32_i32_e32 v100, v100
	v_cvt_f32_i32_e32 v101, v101
	v_cvt_f32_i32_e32 v102, v102
	v_cvt_f32_i32_e32 v103, v103
	v_pk_mul_f32 v[160:161], v[144:145], v[154:155] op_sel_hi:[1,0]
;     __device__ __forceinline__ void operator()(const i32x4 (&acc)[2][2][4][2], const Unit& u, int wr, int wc, int fr, int fq, PG8_LAS unsigned* scr) const {
;     ...
;                 for (int hm = 0; hm < 2; ++hm) { const int m = mp + hm; const int r = ai * HALF + wr * 64 + m * 16 + fr; const float rs = __uint_as_float(scr[r]); float o[8];
; #pragma unroll
;                     for (int n = 0; n < 2; ++n) { const f32x4 sgr = csg[n] * rs, sur = csu[n] * rs;
; #pragma unroll
;                         for (int q = 0; q < 4; ++q) { const float h = fminf(__builtin_fmaf((float)acc[ai][0][m][n][q], sgr[q], bgv[n][q]), 7.0f * C2), up = fminf(fmaxf(__builtin_fmaf((float)acc[ai][1][m][n][q], sur[q], buv[n][q]), -7.0f), 7.0f);
;                             const float sg = __builtin_amdgcn_rcpf(1.0f + __builtin_amdgcn_exp2f(-h)); o[4 * n + q] = __builtin_fmaf(up, ACT_SC / C2, ACT_SC / C2) * (h * sg); } }
;                     int w0 = __builtin_amdgcn_cvt_pk_fp8_f32(o[0], o[1], 0, false); w0 = __builtin_amdgcn_cvt_pk_fp8_f32(o[2], o[3], w0, true);
;                     int w1 = __builtin_amdgcn_cvt_pk_fp8_f32(o[4], o[5], 0, false); w1 = __builtin_amdgcn_cvt_pk_fp8_f32(o[6], o[7], w1, true);
;                     wp[hm][0] = (unsigned)w0; wp[hm][1] = (unsigned)w1; }
	v_pk_mul_f32 v[162:163], v[146:147], v[154:155] op_sel_hi:[1,0]
	v_pk_fma_f32 v[96:97], v[96:97], v[160:161], v[136:137]
	v_pk_fma_f32 v[98:99], v[98:99], v[162:163], v[138:139]
	v_pk_mul_f32 v[160:161], v[148:149], v[154:155] op_sel_hi:[1,0]
	v_pk_mul_f32 v[162:163], v[150:151], v[154:155] op_sel_hi:[1,0]
	v_min_f32_e32 v96, 0x41898193, v96
	v_min_f32_e32 v97, 0x41898193, v97
	v_min_f32_e32 v98, 0x41898193, v98
	v_min_f32_e32 v99, 0x41898193, v99
	v_pk_fma_f32 v[100:101], v[100:101], v[160:161], v[140:141]
	v_pk_fma_f32 v[102:103], v[102:103], v[162:163], v[142:143]
	v_exp_f32_e64 v160, -v96
	v_exp_f32_e64 v161, -v97
	v_exp_f32_e64 v162, -v98
	v_exp_f32_e64 v163, -v99
	v_med3_f32 v100, v100, s8, v199
	v_med3_f32 v101, v101, s8, v199
	v_med3_f32 v102, v102, s8, v199
	v_med3_f32 v103, v103, s8, v199
	v_pk_add_f32 v[160:161], v[160:161], 1.0 op_sel_hi:[1,0]
	v_pk_add_f32 v[162:163], v[162:163], 1.0 op_sel_hi:[1,0]
	v_rcp_f32_e32 v160, v160
	v_rcp_f32_e32 v161, v161
	v_rcp_f32_e32 v162, v162
	v_rcp_f32_e32 v163, v163
	v_pk_fma_f32 v[100:101], v[100:101], s[100:101], s[100:101]
	v_pk_fma_f32 v[102:103], v[102:103], s[100:101], s[100:101]
	v_pk_mul_f32 v[96:97], v[96:97], v[160:161]
	v_pk_mul_f32 v[98:99], v[98:99], v[162:163]
	v_pk_mul_f32 v[96:97], v[100:101], v[96:97]
	v_pk_mul_f32 v[98:99], v[102:103], v[98:99]
	v_cvt_pk_fp8_f32 v96, v96, v97
	v_cvt_pk_fp8_f32 v96, v98, v99 op_sel:[0,0,1]
	v_cvt_f32_i32_e32 v80, v80
	v_cvt_f32_i32_e32 v81, v81
	v_cvt_f32_i32_e32 v82, v82
	v_cvt_f32_i32_e32 v83, v83
	v_cvt_f32_i32_e32 v84, v84
	v_cvt_f32_i32_e32 v85, v85
	v_cvt_f32_i32_e32 v86, v86
	v_cvt_f32_i32_e32 v87, v87
	v_pk_mul_f32 v[202:203], v[144:145], v[154:155] op_sel:[0,1] op_sel_hi:[1,1]
	v_pk_mul_f32 v[204:205], v[146:147], v[154:155] op_sel:[0,1] op_sel_hi:[1,1]
	v_pk_fma_f32 v[80:81], v[80:81], v[202:203], v[136:137]
	v_pk_fma_f32 v[82:83], v[82:83], v[204:205], v[138:139]
	v_pk_mul_f32 v[202:203], v[148:149], v[154:155] op_sel:[0,1] op_sel_hi:[1,1]
	v_pk_mul_f32 v[204:205], v[150:151], v[154:155] op_sel:[0,1] op_sel_hi:[1,1]
	v_min_f32_e32 v80, 0x41898193, v80
	v_min_f32_e32 v81, 0x41898193, v81
	v_min_f32_e32 v82, 0x41898193, v82
	v_min_f32_e32 v83, 0x41898193, v83
	v_pk_fma_f32 v[84:85], v[84:85], v[202:203], v[140:141]
	v_pk_fma_f32 v[86:87], v[86:87], v[204:205], v[142:143]
	v_exp_f32_e64 v202, -v80
	v_exp_f32_e64 v203, -v81
	v_exp_f32_e64 v204, -v82
	v_exp_f32_e64 v205, -v83
	v_med3_f32 v84, v84, s8, v199
	v_med3_f32 v85, v85, s8, v199
	v_med3_f32 v86, v86, s8, v199
	v_med3_f32 v87, v87, s8, v199
	v_pk_add_f32 v[202:203], v[202:203], 1.0 op_sel_hi:[1,0]
	v_pk_add_f32 v[204:205], v[204:205], 1.0 op_sel_hi:[1,0]
	v_rcp_f32_e32 v202, v202
	v_rcp_f32_e32 v203, v203
	v_rcp_f32_e32 v204, v204
	v_rcp_f32_e32 v205, v205
	v_pk_fma_f32 v[84:85], v[84:85], s[100:101], s[100:101]
	v_pk_fma_f32 v[86:87], v[86:87], s[100:101], s[100:101]
	v_pk_mul_f32 v[80:81], v[80:81], v[202:203]
	v_pk_mul_f32 v[82:83], v[82:83], v[204:205]
	v_pk_mul_f32 v[80:81], v[84:85], v[80:81]
	v_pk_mul_f32 v[82:83], v[86:87], v[82:83]
	v_cvt_pk_fp8_f32 v98, v80, v81
	v_cvt_pk_fp8_f32 v98, v82, v83 op_sel:[0,0,1]
	v_cvt_f32_i32_e32 v64, v64
	v_cvt_f32_i32_e32 v65, v65
	v_cvt_f32_i32_e32 v66, v66
	v_cvt_f32_i32_e32 v67, v67
	v_cvt_f32_i32_e32 v68, v68
	v_cvt_f32_i32_e32 v69, v69
	v_cvt_f32_i32_e32 v70, v70
	v_cvt_f32_i32_e32 v71, v71
	v_pk_mul_f32 v[160:161], v[144:145], v[156:157] op_sel_hi:[1,0]
	v_pk_mul_f32 v[162:163], v[146:147], v[156:157] op_sel_hi:[1,0]
	v_pk_fma_f32 v[64:65], v[64:65], v[160:161], v[136:137]
	v_pk_fma_f32 v[66:67], v[66:67], v[162:163], v[138:139]
	v_pk_mul_f32 v[160:161], v[148:149], v[156:157] op_sel_hi:[1,0]
	v_pk_mul_f32 v[162:163], v[150:151], v[156:157] op_sel_hi:[1,0]
	v_min_f32_e32 v64, 0x41898193, v64
	v_min_f32_e32 v65, 0x41898193, v65
	v_min_f32_e32 v66, 0x41898193, v66
	v_min_f32_e32 v67, 0x41898193, v67
	v_pk_fma_f32 v[68:69], v[68:69], v[160:161], v[140:141]
	v_pk_fma_f32 v[70:71], v[70:71], v[162:163], v[142:143]
	v_exp_f32_e64 v160, -v64
	v_exp_f32_e64 v161, -v65
	v_exp_f32_e64 v162, -v66
	v_exp_f32_e64 v163, -v67
	v_med3_f32 v68, v68, s8, v199
	v_med3_f32 v69, v69, s8, v199
	v_med3_f32 v70, v70, s8, v199
	v_med3_f32 v71, v71, s8, v199
	v_pk_add_f32 v[160:161], v[160:161], 1.0 op_sel_hi:[1,0]
	v_pk_add_f32 v[162:163], v[162:163], 1.0 op_sel_hi:[1,0]
	v_rcp_f32_e32 v160, v160
	v_rcp_f32_e32 v161, v161
	v_rcp_f32_e32 v162, v162
	v_rcp_f32_e32 v163, v163
	v_pk_fma_f32 v[68:69], v[68:69], s[100:101], s[100:101]
	v_pk_fma_f32 v[70:71], v[70:71], s[100:101], s[100:101]
	v_pk_mul_f32 v[64:65], v[64:65], v[160:161]
	v_pk_mul_f32 v[66:67], v[66:67], v[162:163]
	v_pk_mul_f32 v[64:65], v[68:69], v[64:65]
	v_pk_mul_f32 v[66:67], v[70:71], v[66:67]
	v_cvt_pk_fp8_f32 v64, v64, v65
	v_cvt_pk_fp8_f32 v64, v66, v67 op_sel:[0,0,1]
	v_cvt_f32_i32_e32 v44, v44
	v_cvt_f32_i32_e32 v45, v45
	v_cvt_f32_i32_e32 v46, v46
	v_cvt_f32_i32_e32 v47, v47
	v_cvt_f32_i32_e32 v48, v48
	v_cvt_f32_i32_e32 v49, v49
	v_cvt_f32_i32_e32 v50, v50
	v_cvt_f32_i32_e32 v51, v51
	v_pk_mul_f32 v[202:203], v[144:145], v[156:157] op_sel:[0,1] op_sel_hi:[1,1]
	v_pk_mul_f32 v[204:205], v[146:147], v[156:157] op_sel:[0,1] op_sel_hi:[1,1]
	v_pk_fma_f32 v[44:45], v[44:45], v[202:203], v[136:137]
	v_pk_fma_f32 v[46:47], v[46:47], v[204:205], v[138:139]
	v_pk_mul_f32 v[202:203], v[148:149], v[156:157] op_sel:[0,1] op_sel_hi:[1,1]
	v_pk_mul_f32 v[204:205], v[150:151], v[156:157] op_sel:[0,1] op_sel_hi:[1,1]
	v_min_f32_e32 v44, 0x41898193, v44
	v_min_f32_e32 v45, 0x41898193, v45
	v_min_f32_e32 v46, 0x41898193, v46
	v_min_f32_e32 v47, 0x41898193, v47
	v_pk_fma_f32 v[48:49], v[48:49], v[202:203], v[140:141]
; #define PG8_LAS __attribute__((address_space(3)))
;     __device__ __forceinline__ void operator()(const i32x4 (&acc)[2][2][4][2], const Unit& u, int wr, int wc, int fr, int fq, PG8_LAS unsigned* scr) const {
;     ...
;         for (int n = 0; n < 2; ++n) { bgv[n] = *(const PG8_LAS f32x4*)(scr + 512 + cl + 4 * n) * C2; buv[n] = *(const PG8_LAS f32x4*)(scr + 512 + 128 + cl + 4 * n);
;             csg[n] = *(const PG8_LAS f32x4*)(scr + 256 + cl + 4 * n) * (C2 / 127.0f); csu[n] = *(const PG8_LAS f32x4*)(scr + 256 + 128 + cl + 4 * n) * (1.0f / 127.0f); }
; #pragma unroll
;         for (int ai = 0; ai < 2; ++ai)
; #pragma unroll
;             for (int mp = 0; mp < 4; mp += 2) { unsigned wp[2][2];
; #pragma unroll
;                 for (int hm = 0; hm < 2; ++hm) { const int m = mp + hm; const int r = ai * HALF + wr * 64 + m * 16 + fr; const float rs = __uint_as_float(scr[r]); float o[8];
; #pragma unroll
;                     for (int n = 0; n < 2; ++n) { const f32x4 sgr = csg[n] * rs, sur = csu[n] * rs;
; #pragma unroll
;                         for (int q = 0; q < 4; ++q) { const float h = fminf(__builtin_fmaf((float)acc[ai][0][m][n][q], sgr[q], bgv[n][q]), 7.0f * C2), up = fminf(fmaxf(__builtin_fmaf((float)acc[ai][1][m][n][q], sur[q], buv[n][q]), -7.0f), 7.0f);
;                             const float sg = __builtin_amdgcn_rcpf(1.0f + __builtin_amdgcn_exp2f(-h)); o[4 * n + q] = __builtin_fmaf(up, ACT_SC / C2, ACT_SC / C2) * (h * sg); } }
;                     int w0 = __builtin_amdgcn_cvt_pk_fp8_f32(o[0], o[1], 0, false); w0 = __builtin_amdgcn_cvt_pk_fp8_f32(o[2], o[3], w0, true);
;                     int w1 = __builtin_amdgcn_cvt_pk_fp8_f32(o[4], o[5], 0, false); w1 = __builtin_amdgcn_cvt_pk_fp8_f32(o[6], o[7], w1, true);
;                     wp[hm][0] = (unsigned)w0; wp[hm][1] = (unsigned)w1; }
	v_pk_fma_f32 v[50:51], v[50:51], v[204:205], v[142:143]
	v_exp_f32_e64 v202, -v44
	v_exp_f32_e64 v203, -v45
	v_exp_f32_e64 v204, -v46
	v_exp_f32_e64 v205, -v47
	v_med3_f32 v48, v48, s8, v199
	v_med3_f32 v49, v49, s8, v199
	v_med3_f32 v50, v50, s8, v199
	v_med3_f32 v51, v51, s8, v199
	v_pk_add_f32 v[202:203], v[202:203], 1.0 op_sel_hi:[1,0]
	v_pk_add_f32 v[204:205], v[204:205], 1.0 op_sel_hi:[1,0]
	v_rcp_f32_e32 v202, v202
	v_rcp_f32_e32 v203, v203
	v_rcp_f32_e32 v204, v204
	v_rcp_f32_e32 v205, v205
	v_pk_fma_f32 v[48:49], v[48:49], s[100:101], s[100:101]
	v_pk_fma_f32 v[50:51], v[50:51], s[100:101], s[100:101]
	v_pk_mul_f32 v[44:45], v[44:45], v[202:203]
	v_pk_mul_f32 v[46:47], v[46:47], v[204:205]
	v_pk_mul_f32 v[44:45], v[48:49], v[44:45]
	v_pk_mul_f32 v[46:47], v[50:51], v[46:47]
	v_cvt_pk_fp8_f32 v66, v44, v45
	v_cvt_pk_fp8_f32 v66, v46, v47 op_sel:[0,0,1]
	v_cvt_f32_i32_e32 v24, v24
	v_cvt_f32_i32_e32 v25, v25
	v_cvt_f32_i32_e32 v26, v26
	v_cvt_f32_i32_e32 v27, v27
	v_cvt_f32_i32_e32 v28, v28
	v_cvt_f32_i32_e32 v29, v29
	v_cvt_f32_i32_e32 v30, v30
	v_cvt_f32_i32_e32 v31, v31
	v_pk_mul_f32 v[160:161], v[144:145], v[158:159] op_sel_hi:[1,0]
	v_pk_mul_f32 v[162:163], v[146:147], v[158:159] op_sel_hi:[1,0]
	v_pk_fma_f32 v[24:25], v[24:25], v[160:161], v[136:137]
	v_pk_fma_f32 v[26:27], v[26:27], v[162:163], v[138:139]
	v_pk_mul_f32 v[160:161], v[148:149], v[158:159] op_sel_hi:[1,0]
	v_pk_mul_f32 v[162:163], v[150:151], v[158:159] op_sel_hi:[1,0]
	v_min_f32_e32 v24, 0x41898193, v24
	v_min_f32_e32 v25, 0x41898193, v25
	v_min_f32_e32 v26, 0x41898193, v26
	v_min_f32_e32 v27, 0x41898193, v27
	v_pk_fma_f32 v[28:29], v[28:29], v[160:161], v[140:141]
	v_pk_fma_f32 v[30:31], v[30:31], v[162:163], v[142:143]
	v_exp_f32_e64 v160, -v24
	v_exp_f32_e64 v161, -v25
	v_exp_f32_e64 v162, -v26
	v_exp_f32_e64 v163, -v27
	v_med3_f32 v28, v28, s8, v199
	v_med3_f32 v29, v29, s8, v199
	v_med3_f32 v30, v30, s8, v199
	v_med3_f32 v31, v31, s8, v199
	v_pk_add_f32 v[160:161], v[160:161], 1.0 op_sel_hi:[1,0]
	v_pk_add_f32 v[162:163], v[162:163], 1.0 op_sel_hi:[1,0]
	v_rcp_f32_e32 v160, v160
	v_rcp_f32_e32 v161, v161
	v_rcp_f32_e32 v162, v162
	v_rcp_f32_e32 v163, v163
	v_pk_fma_f32 v[28:29], v[28:29], s[100:101], s[100:101]
	v_pk_fma_f32 v[30:31], v[30:31], s[100:101], s[100:101]
	v_pk_mul_f32 v[24:25], v[24:25], v[160:161]
	v_pk_mul_f32 v[26:27], v[26:27], v[162:163]
	v_pk_mul_f32 v[24:25], v[28:29], v[24:25]
	v_pk_mul_f32 v[26:27], v[30:31], v[26:27]
	v_cvt_pk_fp8_f32 v24, v24, v25
	v_cvt_pk_fp8_f32 v24, v26, v27 op_sel:[0,0,1]
	v_cvt_f32_i32_e32 v8, v8
	v_cvt_f32_i32_e32 v9, v9
	v_cvt_f32_i32_e32 v10, v10
	v_cvt_f32_i32_e32 v11, v11
	v_cvt_f32_i32_e32 v12, v12
	v_cvt_f32_i32_e32 v13, v13
	v_cvt_f32_i32_e32 v14, v14
	v_cvt_f32_i32_e32 v15, v15
	v_pk_mul_f32 v[202:203], v[144:145], v[158:159] op_sel:[0,1] op_sel_hi:[1,1]
	v_pk_mul_f32 v[204:205], v[146:147], v[158:159] op_sel:[0,1] op_sel_hi:[1,1]
	v_pk_fma_f32 v[8:9], v[8:9], v[202:203], v[136:137]
	v_pk_fma_f32 v[10:11], v[10:11], v[204:205], v[138:139]
	v_pk_mul_f32 v[202:203], v[148:149], v[158:159] op_sel:[0,1] op_sel_hi:[1,1]
	v_pk_mul_f32 v[204:205], v[150:151], v[158:159] op_sel:[0,1] op_sel_hi:[1,1]
	v_min_f32_e32 v8, 0x41898193, v8
	v_min_f32_e32 v9, 0x41898193, v9
	v_min_f32_e32 v10, 0x41898193, v10
	v_min_f32_e32 v11, 0x41898193, v11
	v_pk_fma_f32 v[12:13], v[12:13], v[202:203], v[140:141]
	v_pk_fma_f32 v[14:15], v[14:15], v[204:205], v[142:143]
	v_exp_f32_e64 v202, -v8
	v_exp_f32_e64 v203, -v9
	v_exp_f32_e64 v204, -v10
	v_exp_f32_e64 v205, -v11
	v_med3_f32 v12, v12, s8, v199
	v_med3_f32 v13, v13, s8, v199
	v_med3_f32 v14, v14, s8, v199
	v_med3_f32 v15, v15, s8, v199
	v_pk_add_f32 v[202:203], v[202:203], 1.0 op_sel_hi:[1,0]
	v_pk_add_f32 v[204:205], v[204:205], 1.0 op_sel_hi:[1,0]
	v_rcp_f32_e32 v202, v202
	v_rcp_f32_e32 v203, v203
	v_rcp_f32_e32 v204, v204
	v_rcp_f32_e32 v205, v205
	v_pk_fma_f32 v[12:13], v[12:13], s[100:101], s[100:101]
	v_pk_fma_f32 v[14:15], v[14:15], s[100:101], s[100:101]
	v_pk_mul_f32 v[8:9], v[8:9], v[202:203]
	v_pk_mul_f32 v[10:11], v[10:11], v[204:205]
	v_pk_mul_f32 v[8:9], v[12:13], v[8:9]
	v_pk_mul_f32 v[10:11], v[14:15], v[10:11]
	v_cvt_pk_fp8_f32 v26, v8, v9
	v_cvt_pk_fp8_f32 v26, v10, v11 op_sel:[0,0,1]
	v_add_u32_e32 v160, 0x20d10, v208
	ds_read_b128 v[136:139], v160 offset:1024
	ds_read_b128 v[140:143], v160 offset:1536
	ds_read_b128 v[144:147], v160
	ds_read_b128 v[148:151], v160 offset:512
	s_waitcnt lgkmcnt(0)
; #define GAS __attribute__((address_space(1)))
;     __device__ __forceinline__ void operator()(const i32x4 (&acc)[2][2][4][2], const Unit& u, int wr, int wc, int fr, int fq, PG8_LAS unsigned* scr) const {
;     ...
;                 for (int hm = 0; hm < 2; ++hm) { const int m = mp + hm; const int r = ai * HALF + wr * 64 + m * 16 + fr; const float rs = __uint_as_float(scr[r]); float o[8];
; #pragma unroll
;                     for (int n = 0; n < 2; ++n) { const f32x4 sgr = csg[n] * rs, sur = csu[n] * rs;
; #pragma unroll
;                         for (int q = 0; q < 4; ++q) { const float h = fminf(__builtin_fmaf((float)acc[ai][0][m][n][q], sgr[q], bgv[n][q]), 7.0f * C2), up = fminf(fmaxf(__builtin_fmaf((float)acc[ai][1][m][n][q], sur[q], buv[n][q]), -7.0f), 7.0f);
;                             const float sg = __builtin_amdgcn_rcpf(1.0f + __builtin_amdgcn_exp2f(-h)); o[4 * n + q] = __builtin_fmaf(up, ACT_SC / C2, ACT_SC / C2) * (h * sg); } }
;                     int w0 = __builtin_amdgcn_cvt_pk_fp8_f32(o[0], o[1], 0, false); w0 = __builtin_amdgcn_cvt_pk_fp8_f32(o[2], o[3], w0, true);
;                     int w1 = __builtin_amdgcn_cvt_pk_fp8_f32(o[4], o[5], 0, false); w1 = __builtin_amdgcn_cvt_pk_fp8_f32(o[6], o[7], w1, true);
;                     wp[hm][0] = (unsigned)w0; wp[hm][1] = (unsigned)w1; }
;                 { auto r0 = __builtin_amdgcn_permlane16_swap(wp[0][0], wp[1][0], false, false); wp[0][0] = r0[0]; wp[1][0] = r0[1];
;                   auto r1 = __builtin_amdgcn_permlane16_swap(wp[0][1], wp[1][1], false, false); wp[0][1] = r1[0]; wp[1][1] = r1[1]; }
;                 const int odd = fq & 1;
;                 const size_t arow = (size_t)(row0 + ai * HALF + (mp + odd) * 16);
;                 *(GAS u32x4*)(act + arow * 1024 + (c0 - 8 * odd)) = (u32x4){wp[0][0], wp[0][1], wp[1][0], wp[1][1]};
	v_mul_f32_e32 v136, 0x401d265f, v136
	v_mul_f32_e32 v137, 0x401d265f, v137
	v_mul_f32_e32 v138, 0x401d265f, v138
	v_mul_f32_e32 v139, 0x401d265f, v139
	v_mul_f32_e32 v144, 0x3c9e6325, v144
	v_mul_f32_e32 v145, 0x3c9e6325, v145
	v_mul_f32_e32 v146, 0x3c9e6325, v146
	v_mul_f32_e32 v147, 0x3c9e6325, v147
	v_mul_f32_e32 v148, 0x3c010204, v148
	v_mul_f32_e32 v149, 0x3c010204, v149
	v_mul_f32_e32 v150, 0x3c010204, v150
	v_mul_f32_e32 v151, 0x3c010204, v151
	v_cvt_f32_i32_e32 v120, v120
	v_cvt_f32_i32_e32 v121, v121
	v_cvt_f32_i32_e32 v122, v122
	v_cvt_f32_i32_e32 v123, v123
	v_cvt_f32_i32_e32 v124, v124
	v_cvt_f32_i32_e32 v125, v125
	v_cvt_f32_i32_e32 v126, v126
	v_cvt_f32_i32_e32 v127, v127
	v_pk_mul_f32 v[160:161], v[144:145], v[152:153] op_sel_hi:[1,0]
	v_pk_mul_f32 v[162:163], v[146:147], v[152:153] op_sel_hi:[1,0]
	v_pk_fma_f32 v[120:121], v[120:121], v[160:161], v[136:137]
	v_pk_fma_f32 v[122:123], v[122:123], v[162:163], v[138:139]
	v_pk_mul_f32 v[160:161], v[148:149], v[152:153] op_sel_hi:[1,0]
	v_pk_mul_f32 v[162:163], v[150:151], v[152:153] op_sel_hi:[1,0]
	v_min_f32_e32 v120, 0x41898193, v120
	v_min_f32_e32 v121, 0x41898193, v121
	v_min_f32_e32 v122, 0x41898193, v122
	v_min_f32_e32 v123, 0x41898193, v123
	v_pk_fma_f32 v[124:125], v[124:125], v[160:161], v[140:141]
	v_pk_fma_f32 v[126:127], v[126:127], v[162:163], v[142:143]
	v_exp_f32_e64 v160, -v120
	v_exp_f32_e64 v161, -v121
	v_exp_f32_e64 v162, -v122
	v_exp_f32_e64 v163, -v123
	v_med3_f32 v124, v124, s8, v199
	v_med3_f32 v125, v125, s8, v199
	v_med3_f32 v126, v126, s8, v199
	v_med3_f32 v127, v127, s8, v199
	v_pk_add_f32 v[160:161], v[160:161], 1.0 op_sel_hi:[1,0]
	v_pk_add_f32 v[162:163], v[162:163], 1.0 op_sel_hi:[1,0]
	v_rcp_f32_e32 v160, v160
	v_rcp_f32_e32 v161, v161
	v_rcp_f32_e32 v162, v162
	v_rcp_f32_e32 v163, v163
	v_pk_fma_f32 v[124:125], v[124:125], s[100:101], s[100:101]
	v_pk_fma_f32 v[126:127], v[126:127], s[100:101], s[100:101]
	v_pk_mul_f32 v[120:121], v[120:121], v[160:161]
	v_pk_mul_f32 v[122:123], v[122:123], v[162:163]
	v_pk_mul_f32 v[120:121], v[124:125], v[120:121]
	v_pk_mul_f32 v[122:123], v[126:127], v[122:123]
	v_cvt_pk_fp8_f32 v129, v120, v121
	v_cvt_pk_fp8_f32 v129, v122, v123 op_sel:[0,0,1]
	v_cvt_f32_i32_e32 v104, v104
	v_cvt_f32_i32_e32 v105, v105
	v_cvt_f32_i32_e32 v106, v106
	v_cvt_f32_i32_e32 v107, v107
	v_cvt_f32_i32_e32 v108, v108
	v_cvt_f32_i32_e32 v109, v109
	v_cvt_f32_i32_e32 v110, v110
	v_cvt_f32_i32_e32 v111, v111
	v_pk_mul_f32 v[202:203], v[144:145], v[152:153] op_sel:[0,1] op_sel_hi:[1,1]
	v_pk_mul_f32 v[204:205], v[146:147], v[152:153] op_sel:[0,1] op_sel_hi:[1,1]
	v_pk_fma_f32 v[104:105], v[104:105], v[202:203], v[136:137]
	v_pk_fma_f32 v[106:107], v[106:107], v[204:205], v[138:139]
	v_pk_mul_f32 v[202:203], v[148:149], v[152:153] op_sel:[0,1] op_sel_hi:[1,1]
	v_pk_mul_f32 v[204:205], v[150:151], v[152:153] op_sel:[0,1] op_sel_hi:[1,1]
	v_min_f32_e32 v104, 0x41898193, v104
	v_min_f32_e32 v105, 0x41898193, v105
	v_min_f32_e32 v106, 0x41898193, v106
	v_min_f32_e32 v107, 0x41898193, v107
	v_pk_fma_f32 v[108:109], v[108:109], v[202:203], v[140:141]
	v_pk_fma_f32 v[110:111], v[110:111], v[204:205], v[142:143]
	v_exp_f32_e64 v202, -v104
	v_exp_f32_e64 v203, -v105
	v_exp_f32_e64 v204, -v106
	v_exp_f32_e64 v205, -v107
	v_med3_f32 v108, v108, s8, v199
	v_med3_f32 v109, v109, s8, v199
	v_med3_f32 v110, v110, s8, v199
	v_med3_f32 v111, v111, s8, v199
	v_pk_add_f32 v[202:203], v[202:203], 1.0 op_sel_hi:[1,0]
	v_pk_add_f32 v[204:205], v[204:205], 1.0 op_sel_hi:[1,0]
	v_rcp_f32_e32 v202, v202
	v_rcp_f32_e32 v203, v203
	v_rcp_f32_e32 v204, v204
	v_rcp_f32_e32 v205, v205
	v_pk_fma_f32 v[108:109], v[108:109], s[100:101], s[100:101]
	v_pk_fma_f32 v[110:111], v[110:111], s[100:101], s[100:101]
	v_pk_mul_f32 v[104:105], v[104:105], v[202:203]
	v_pk_mul_f32 v[106:107], v[106:107], v[204:205]
	v_pk_mul_f32 v[104:105], v[108:109], v[104:105]
	v_pk_mul_f32 v[106:107], v[110:111], v[106:107]
	v_cvt_pk_fp8_f32 v131, v104, v105
	v_cvt_pk_fp8_f32 v131, v106, v107 op_sel:[0,0,1]
	s_nop 1
	v_permlane16_swap_b32_e32 v128, v130
	v_permlane16_swap_b32_e32 v129, v131
	global_store_dwordx4 v207, v[128:131], s[60:61]
	v_cvt_f32_i32_e32 v88, v88
	v_cvt_f32_i32_e32 v89, v89
	v_cvt_f32_i32_e32 v90, v90
	v_cvt_f32_i32_e32 v91, v91
	v_cvt_f32_i32_e32 v92, v92
	v_cvt_f32_i32_e32 v93, v93
	v_cvt_f32_i32_e32 v94, v94
	v_cvt_f32_i32_e32 v95, v95
	v_pk_mul_f32 v[160:161], v[144:145], v[154:155] op_sel_hi:[1,0]
	v_pk_mul_f32 v[162:163], v[146:147], v[154:155] op_sel_hi:[1,0]
	v_pk_fma_f32 v[88:89], v[88:89], v[160:161], v[136:137]
	v_pk_fma_f32 v[90:91], v[90:91], v[162:163], v[138:139]
	v_pk_mul_f32 v[160:161], v[148:149], v[154:155] op_sel_hi:[1,0]
	v_pk_mul_f32 v[162:163], v[150:151], v[154:155] op_sel_hi:[1,0]
	v_min_f32_e32 v88, 0x41898193, v88
	v_min_f32_e32 v89, 0x41898193, v89
	v_min_f32_e32 v90, 0x41898193, v90
	v_min_f32_e32 v91, 0x41898193, v91
	v_pk_fma_f32 v[92:93], v[92:93], v[160:161], v[140:141]
	v_pk_fma_f32 v[94:95], v[94:95], v[162:163], v[142:143]
	v_exp_f32_e64 v160, -v88
	v_exp_f32_e64 v161, -v89
	v_exp_f32_e64 v162, -v90
	v_exp_f32_e64 v163, -v91
	v_med3_f32 v92, v92, s8, v199
	v_med3_f32 v93, v93, s8, v199
	v_med3_f32 v94, v94, s8, v199
	v_med3_f32 v95, v95, s8, v199
	v_pk_add_f32 v[160:161], v[160:161], 1.0 op_sel_hi:[1,0]
	v_pk_add_f32 v[162:163], v[162:163], 1.0 op_sel_hi:[1,0]
	v_rcp_f32_e32 v160, v160
	v_rcp_f32_e32 v161, v161
	v_rcp_f32_e32 v162, v162
	v_rcp_f32_e32 v163, v163
	v_pk_fma_f32 v[92:93], v[92:93], s[100:101], s[100:101]
	v_pk_fma_f32 v[94:95], v[94:95], s[100:101], s[100:101]
	v_pk_mul_f32 v[88:89], v[88:89], v[160:161]
; #define GAS __attribute__((address_space(1)))
;     __device__ __forceinline__ void operator()(const i32x4 (&acc)[2][2][4][2], const Unit& u, int wr, int wc, int fr, int fq, PG8_LAS unsigned* scr) const {
;     ...
;                 for (int hm = 0; hm < 2; ++hm) { const int m = mp + hm; const int r = ai * HALF + wr * 64 + m * 16 + fr; const float rs = __uint_as_float(scr[r]); float o[8];
; #pragma unroll
;                     for (int n = 0; n < 2; ++n) { const f32x4 sgr = csg[n] * rs, sur = csu[n] * rs;
; #pragma unroll
;                         for (int q = 0; q < 4; ++q) { const float h = fminf(__builtin_fmaf((float)acc[ai][0][m][n][q], sgr[q], bgv[n][q]), 7.0f * C2), up = fminf(fmaxf(__builtin_fmaf((float)acc[ai][1][m][n][q], sur[q], buv[n][q]), -7.0f), 7.0f);
;                             const float sg = __builtin_amdgcn_rcpf(1.0f + __builtin_amdgcn_exp2f(-h)); o[4 * n + q] = __builtin_fmaf(up, ACT_SC / C2, ACT_SC / C2) * (h * sg); } }
;                     int w0 = __builtin_amdgcn_cvt_pk_fp8_f32(o[0], o[1], 0, false); w0 = __builtin_amdgcn_cvt_pk_fp8_f32(o[2], o[3], w0, true);
;                     int w1 = __builtin_amdgcn_cvt_pk_fp8_f32(o[4], o[5], 0, false); w1 = __builtin_amdgcn_cvt_pk_fp8_f32(o[6], o[7], w1, true);
;                     wp[hm][0] = (unsigned)w0; wp[hm][1] = (unsigned)w1; }
;                 { auto r0 = __builtin_amdgcn_permlane16_swap(wp[0][0], wp[1][0], false, false); wp[0][0] = r0[0]; wp[1][0] = r0[1];
;                   auto r1 = __builtin_amdgcn_permlane16_swap(wp[0][1], wp[1][1], false, false); wp[0][1] = r1[0]; wp[1][1] = r1[1]; }
;                 const int odd = fq & 1;
;                 const size_t arow = (size_t)(row0 + ai * HALF + (mp + odd) * 16);
;                 *(GAS u32x4*)(act + arow * 1024 + (c0 - 8 * odd)) = (u32x4){wp[0][0], wp[0][1], wp[1][0], wp[1][1]};
	v_pk_mul_f32 v[90:91], v[90:91], v[162:163]
	v_pk_mul_f32 v[88:89], v[92:93], v[88:89]
	v_pk_mul_f32 v[90:91], v[94:95], v[90:91]
	v_cvt_pk_fp8_f32 v97, v88, v89
	v_cvt_pk_fp8_f32 v97, v90, v91 op_sel:[0,0,1]
	v_cvt_f32_i32_e32 v72, v72
	v_cvt_f32_i32_e32 v73, v73
	v_cvt_f32_i32_e32 v74, v74
	v_cvt_f32_i32_e32 v75, v75
	v_cvt_f32_i32_e32 v76, v76
	v_cvt_f32_i32_e32 v77, v77
	v_cvt_f32_i32_e32 v78, v78
	v_cvt_f32_i32_e32 v79, v79
	v_pk_mul_f32 v[202:203], v[144:145], v[154:155] op_sel:[0,1] op_sel_hi:[1,1]
	v_pk_mul_f32 v[204:205], v[146:147], v[154:155] op_sel:[0,1] op_sel_hi:[1,1]
	v_pk_fma_f32 v[72:73], v[72:73], v[202:203], v[136:137]
	v_pk_fma_f32 v[74:75], v[74:75], v[204:205], v[138:139]
	v_pk_mul_f32 v[202:203], v[148:149], v[154:155] op_sel:[0,1] op_sel_hi:[1,1]
	v_pk_mul_f32 v[204:205], v[150:151], v[154:155] op_sel:[0,1] op_sel_hi:[1,1]
	v_min_f32_e32 v72, 0x41898193, v72
	v_min_f32_e32 v73, 0x41898193, v73
	v_min_f32_e32 v74, 0x41898193, v74
	v_min_f32_e32 v75, 0x41898193, v75
	v_pk_fma_f32 v[76:77], v[76:77], v[202:203], v[140:141]
	v_pk_fma_f32 v[78:79], v[78:79], v[204:205], v[142:143]
	v_exp_f32_e64 v202, -v72
	v_exp_f32_e64 v203, -v73
	v_exp_f32_e64 v204, -v74
	v_exp_f32_e64 v205, -v75
	v_med3_f32 v76, v76, s8, v199
	v_med3_f32 v77, v77, s8, v199
	v_med3_f32 v78, v78, s8, v199
	v_med3_f32 v79, v79, s8, v199
	v_pk_add_f32 v[202:203], v[202:203], 1.0 op_sel_hi:[1,0]
	v_pk_add_f32 v[204:205], v[204:205], 1.0 op_sel_hi:[1,0]
	v_rcp_f32_e32 v202, v202
	v_rcp_f32_e32 v203, v203
	v_rcp_f32_e32 v204, v204
	v_rcp_f32_e32 v205, v205
	v_pk_fma_f32 v[76:77], v[76:77], s[100:101], s[100:101]
	v_pk_fma_f32 v[78:79], v[78:79], s[100:101], s[100:101]
	v_pk_mul_f32 v[72:73], v[72:73], v[202:203]
	v_pk_mul_f32 v[74:75], v[74:75], v[204:205]
	v_pk_mul_f32 v[72:73], v[76:77], v[72:73]
	v_pk_mul_f32 v[74:75], v[78:79], v[74:75]
	v_cvt_pk_fp8_f32 v99, v72, v73
	v_cvt_pk_fp8_f32 v99, v74, v75 op_sel:[0,0,1]
	s_nop 1
	v_permlane16_swap_b32_e32 v96, v98
	v_permlane16_swap_b32_e32 v97, v99
	v_add_u32_e32 v160, 0x8000, v207
	global_store_dwordx4 v160, v[96:99], s[60:61]
	v_cvt_f32_i32_e32 v56, v56
	v_cvt_f32_i32_e32 v57, v57
	v_cvt_f32_i32_e32 v58, v58
	v_cvt_f32_i32_e32 v59, v59
	v_cvt_f32_i32_e32 v60, v60
	v_cvt_f32_i32_e32 v61, v61
	v_cvt_f32_i32_e32 v62, v62
	v_cvt_f32_i32_e32 v63, v63
	v_pk_mul_f32 v[160:161], v[144:145], v[156:157] op_sel_hi:[1,0]
	v_pk_mul_f32 v[162:163], v[146:147], v[156:157] op_sel_hi:[1,0]
	v_pk_fma_f32 v[56:57], v[56:57], v[160:161], v[136:137]
	v_pk_fma_f32 v[58:59], v[58:59], v[162:163], v[138:139]
	v_pk_mul_f32 v[160:161], v[148:149], v[156:157] op_sel_hi:[1,0]
	v_pk_mul_f32 v[162:163], v[150:151], v[156:157] op_sel_hi:[1,0]
	v_min_f32_e32 v56, 0x41898193, v56
	v_min_f32_e32 v57, 0x41898193, v57
	v_min_f32_e32 v58, 0x41898193, v58
	v_min_f32_e32 v59, 0x41898193, v59
	v_pk_fma_f32 v[60:61], v[60:61], v[160:161], v[140:141]
	v_pk_fma_f32 v[62:63], v[62:63], v[162:163], v[142:143]
	v_exp_f32_e64 v160, -v56
	v_exp_f32_e64 v161, -v57
	v_exp_f32_e64 v162, -v58
	v_exp_f32_e64 v163, -v59
	v_med3_f32 v60, v60, s8, v199
	v_med3_f32 v61, v61, s8, v199
	v_med3_f32 v62, v62, s8, v199
	v_med3_f32 v63, v63, s8, v199
	v_pk_add_f32 v[160:161], v[160:161], 1.0 op_sel_hi:[1,0]
	v_pk_add_f32 v[162:163], v[162:163], 1.0 op_sel_hi:[1,0]
	v_rcp_f32_e32 v160, v160
	v_rcp_f32_e32 v161, v161
	v_rcp_f32_e32 v162, v162
	v_rcp_f32_e32 v163, v163
	v_pk_fma_f32 v[60:61], v[60:61], s[100:101], s[100:101]
	v_pk_fma_f32 v[62:63], v[62:63], s[100:101], s[100:101]
	v_pk_mul_f32 v[56:57], v[56:57], v[160:161]
	v_pk_mul_f32 v[58:59], v[58:59], v[162:163]
	v_pk_mul_f32 v[56:57], v[60:61], v[56:57]
	v_pk_mul_f32 v[58:59], v[62:63], v[58:59]
	v_cvt_pk_fp8_f32 v65, v56, v57
	v_cvt_pk_fp8_f32 v65, v58, v59 op_sel:[0,0,1]
	v_cvt_f32_i32_e32 v32, v32
	v_cvt_f32_i32_e32 v33, v33
	v_cvt_f32_i32_e32 v34, v34
	v_cvt_f32_i32_e32 v35, v35
	v_cvt_f32_i32_e32 v36, v36
	v_cvt_f32_i32_e32 v37, v37
	v_cvt_f32_i32_e32 v38, v38
	v_cvt_f32_i32_e32 v39, v39
	v_pk_mul_f32 v[202:203], v[144:145], v[156:157] op_sel:[0,1] op_sel_hi:[1,1]
	v_pk_mul_f32 v[204:205], v[146:147], v[156:157] op_sel:[0,1] op_sel_hi:[1,1]
	v_pk_fma_f32 v[32:33], v[32:33], v[202:203], v[136:137]
	v_pk_fma_f32 v[34:35], v[34:35], v[204:205], v[138:139]
	v_pk_mul_f32 v[202:203], v[148:149], v[156:157] op_sel:[0,1] op_sel_hi:[1,1]
	v_pk_mul_f32 v[204:205], v[150:151], v[156:157] op_sel:[0,1] op_sel_hi:[1,1]
	v_min_f32_e32 v32, 0x41898193, v32
	v_min_f32_e32 v33, 0x41898193, v33
	v_min_f32_e32 v34, 0x41898193, v34
	v_min_f32_e32 v35, 0x41898193, v35
	v_pk_fma_f32 v[36:37], v[36:37], v[202:203], v[140:141]
	v_pk_fma_f32 v[38:39], v[38:39], v[204:205], v[142:143]
	v_exp_f32_e64 v202, -v32
	v_exp_f32_e64 v203, -v33
	v_exp_f32_e64 v204, -v34
	v_exp_f32_e64 v205, -v35
	v_med3_f32 v36, v36, s8, v199
	v_med3_f32 v37, v37, s8, v199
	v_med3_f32 v38, v38, s8, v199
	v_med3_f32 v39, v39, s8, v199
; #define GAS __attribute__((address_space(1)))
; #define PG8_BAR __builtin_amdgcn_s_barrier()
;     __device__ __forceinline__ void operator()(const i32x4 (&acc)[2][2][4][2], const Unit& u, int wr, int wc, int fr, int fq, PG8_LAS unsigned* scr) const {
;     ...
;                 for (int hm = 0; hm < 2; ++hm) { const int m = mp + hm; const int r = ai * HALF + wr * 64 + m * 16 + fr; const float rs = __uint_as_float(scr[r]); float o[8];
; #pragma unroll
;                     for (int n = 0; n < 2; ++n) { const f32x4 sgr = csg[n] * rs, sur = csu[n] * rs;
; #pragma unroll
;                         for (int q = 0; q < 4; ++q) { const float h = fminf(__builtin_fmaf((float)acc[ai][0][m][n][q], sgr[q], bgv[n][q]), 7.0f * C2), up = fminf(fmaxf(__builtin_fmaf((float)acc[ai][1][m][n][q], sur[q], buv[n][q]), -7.0f), 7.0f);
;                             const float sg = __builtin_amdgcn_rcpf(1.0f + __builtin_amdgcn_exp2f(-h)); o[4 * n + q] = __builtin_fmaf(up, ACT_SC / C2, ACT_SC / C2) * (h * sg); } }
;                     int w0 = __builtin_amdgcn_cvt_pk_fp8_f32(o[0], o[1], 0, false); w0 = __builtin_amdgcn_cvt_pk_fp8_f32(o[2], o[3], w0, true);
;                     int w1 = __builtin_amdgcn_cvt_pk_fp8_f32(o[4], o[5], 0, false); w1 = __builtin_amdgcn_cvt_pk_fp8_f32(o[6], o[7], w1, true);
;                     wp[hm][0] = (unsigned)w0; wp[hm][1] = (unsigned)w1; }
;                 { auto r0 = __builtin_amdgcn_permlane16_swap(wp[0][0], wp[1][0], false, false); wp[0][0] = r0[0]; wp[1][0] = r0[1];
;                   auto r1 = __builtin_amdgcn_permlane16_swap(wp[0][1], wp[1][1], false, false); wp[0][1] = r1[0]; wp[1][1] = r1[1]; }
;                 const int odd = fq & 1;
;                 const size_t arow = (size_t)(row0 + ai * HALF + (mp + odd) * 16);
;                 *(GAS u32x4*)(act + arow * 1024 + (c0 - 8 * odd)) = (u32x4){wp[0][0], wp[0][1], wp[1][0], wp[1][1]};
;                 __builtin_amdgcn_sched_barrier(0); }
; template <class Epi, class Sched, bool GATHER, int MODE>
; __device__ __forceinline__ void gemm_phase(PG8_LAS unsigned char* lds, PG8_LAS unsigned* scr, const Gemm g, const Sched& S, const Epi& E, int tid_in) {
;     ...
;         if (!has_next) break;
;         cur = nxt; cA = nA; cB = nB; ++ui;
;         if (GATHER) { const u32x4 nx = gather_read(cur); c0[0] = nx[0]; c0[1] = nx[1]; c1[0] = nx[2]; c1[1] = nx[3]; }
;         if (wr == 1) PG8_BAR;
	v_pk_add_f32 v[202:203], v[202:203], 1.0 op_sel_hi:[1,0]
	v_pk_add_f32 v[204:205], v[204:205], 1.0 op_sel_hi:[1,0]
	v_rcp_f32_e32 v202, v202
	v_rcp_f32_e32 v203, v203
	v_rcp_f32_e32 v204, v204
	v_rcp_f32_e32 v205, v205
	v_pk_fma_f32 v[36:37], v[36:37], s[100:101], s[100:101]
	v_pk_fma_f32 v[38:39], v[38:39], s[100:101], s[100:101]
	v_pk_mul_f32 v[32:33], v[32:33], v[202:203]
	v_pk_mul_f32 v[34:35], v[34:35], v[204:205]
	v_pk_mul_f32 v[32:33], v[36:37], v[32:33]
	v_pk_mul_f32 v[34:35], v[38:39], v[34:35]
	v_cvt_pk_fp8_f32 v67, v32, v33
	v_cvt_pk_fp8_f32 v67, v34, v35 op_sel:[0,0,1]
	s_nop 1
	v_permlane16_swap_b32_e32 v64, v66
	v_permlane16_swap_b32_e32 v65, v67
	v_add_u32_e32 v160, 0x20000, v207
	global_store_dwordx4 v160, v[64:67], s[60:61]
	v_cvt_f32_i32_e32 v16, v16
	v_cvt_f32_i32_e32 v17, v17
	v_cvt_f32_i32_e32 v18, v18
	v_cvt_f32_i32_e32 v19, v19
	v_cvt_f32_i32_e32 v20, v20
	v_cvt_f32_i32_e32 v21, v21
	v_cvt_f32_i32_e32 v22, v22
	v_cvt_f32_i32_e32 v23, v23
	v_pk_mul_f32 v[160:161], v[144:145], v[158:159] op_sel_hi:[1,0]
	v_pk_mul_f32 v[162:163], v[146:147], v[158:159] op_sel_hi:[1,0]
	v_pk_fma_f32 v[16:17], v[16:17], v[160:161], v[136:137]
	v_pk_fma_f32 v[18:19], v[18:19], v[162:163], v[138:139]
	v_pk_mul_f32 v[160:161], v[148:149], v[158:159] op_sel_hi:[1,0]
	v_pk_mul_f32 v[162:163], v[150:151], v[158:159] op_sel_hi:[1,0]
	v_min_f32_e32 v16, 0x41898193, v16
	v_min_f32_e32 v17, 0x41898193, v17
	v_min_f32_e32 v18, 0x41898193, v18
	v_min_f32_e32 v19, 0x41898193, v19
	v_pk_fma_f32 v[20:21], v[20:21], v[160:161], v[140:141]
	v_pk_fma_f32 v[22:23], v[22:23], v[162:163], v[142:143]
	v_exp_f32_e64 v160, -v16
	v_exp_f32_e64 v161, -v17
	v_exp_f32_e64 v162, -v18
	v_exp_f32_e64 v163, -v19
	v_med3_f32 v20, v20, s8, v199
	v_med3_f32 v21, v21, s8, v199
	v_med3_f32 v22, v22, s8, v199
	v_med3_f32 v23, v23, s8, v199
	v_pk_add_f32 v[160:161], v[160:161], 1.0 op_sel_hi:[1,0]
	v_pk_add_f32 v[162:163], v[162:163], 1.0 op_sel_hi:[1,0]
	v_rcp_f32_e32 v160, v160
	v_rcp_f32_e32 v161, v161
	v_rcp_f32_e32 v162, v162
	v_rcp_f32_e32 v163, v163
	v_pk_fma_f32 v[20:21], v[20:21], s[100:101], s[100:101]
	v_pk_fma_f32 v[22:23], v[22:23], s[100:101], s[100:101]
	v_pk_mul_f32 v[16:17], v[16:17], v[160:161]
	v_pk_mul_f32 v[18:19], v[18:19], v[162:163]
	v_pk_mul_f32 v[16:17], v[20:21], v[16:17]
	v_pk_mul_f32 v[18:19], v[22:23], v[18:19]
	v_cvt_pk_fp8_f32 v25, v16, v17
	v_cvt_pk_fp8_f32 v25, v18, v19 op_sel:[0,0,1]
	v_cvt_f32_i32_e32 v0, v0
	v_cvt_f32_i32_e32 v1, v1
	v_cvt_f32_i32_e32 v2, v2
	v_cvt_f32_i32_e32 v3, v3
	v_cvt_f32_i32_e32 v4, v4
	v_cvt_f32_i32_e32 v5, v5
	v_cvt_f32_i32_e32 v6, v6
	v_cvt_f32_i32_e32 v7, v7
	v_pk_mul_f32 v[202:203], v[144:145], v[158:159] op_sel:[0,1] op_sel_hi:[1,1]
	v_pk_mul_f32 v[204:205], v[146:147], v[158:159] op_sel:[0,1] op_sel_hi:[1,1]
	v_pk_fma_f32 v[0:1], v[0:1], v[202:203], v[136:137]
	v_pk_fma_f32 v[2:3], v[2:3], v[204:205], v[138:139]
	v_pk_mul_f32 v[202:203], v[148:149], v[158:159] op_sel:[0,1] op_sel_hi:[1,1]
	v_pk_mul_f32 v[204:205], v[150:151], v[158:159] op_sel:[0,1] op_sel_hi:[1,1]
	v_min_f32_e32 v0, 0x41898193, v0
	v_min_f32_e32 v1, 0x41898193, v1
	v_min_f32_e32 v2, 0x41898193, v2
	v_min_f32_e32 v3, 0x41898193, v3
	v_pk_fma_f32 v[4:5], v[4:5], v[202:203], v[140:141]
	v_pk_fma_f32 v[6:7], v[6:7], v[204:205], v[142:143]
	v_exp_f32_e64 v202, -v0
	v_exp_f32_e64 v203, -v1
	v_exp_f32_e64 v204, -v2
	v_exp_f32_e64 v205, -v3
	v_med3_f32 v4, v4, s8, v199
	v_med3_f32 v5, v5, s8, v199
	v_med3_f32 v6, v6, s8, v199
	v_med3_f32 v7, v7, s8, v199
	v_pk_add_f32 v[202:203], v[202:203], 1.0 op_sel_hi:[1,0]
	v_pk_add_f32 v[204:205], v[204:205], 1.0 op_sel_hi:[1,0]
	v_rcp_f32_e32 v202, v202
	v_rcp_f32_e32 v203, v203
	v_rcp_f32_e32 v204, v204
	v_rcp_f32_e32 v205, v205
	v_pk_fma_f32 v[4:5], v[4:5], s[100:101], s[100:101]
	v_pk_fma_f32 v[6:7], v[6:7], s[100:101], s[100:101]
	v_pk_mul_f32 v[0:1], v[0:1], v[202:203]
	v_pk_mul_f32 v[2:3], v[2:3], v[204:205]
	v_pk_mul_f32 v[0:1], v[4:5], v[0:1]
	v_pk_mul_f32 v[2:3], v[6:7], v[2:3]
	v_cvt_pk_fp8_f32 v27, v0, v1
	v_cvt_pk_fp8_f32 v27, v2, v3 op_sel:[0,0,1]
	s_nop 1
	v_permlane16_swap_b32_e32 v24, v26
	v_permlane16_swap_b32_e32 v25, v27
	v_add_u32_e32 v160, 0x28000, v207
	global_store_dwordx4 v160, v[24:27], s[60:61]
	s_cmp_eq_u32 s38, s89
	s_mov_b64 s[10:11], -1
	s_cbranch_scc1 .LBB0_786
	s_andn2_b64 vcc, exec, s[58:59]
	s_cbranch_vccnz .LBB0_785
	s_barrier
	s_branch .LBB0_785
	s_nop 0
	s_nop 0
	s_nop 0
	s_nop 0
	s_nop 0
	s_nop 0
	s_nop 0
	s_nop 0
	s_nop 0
	s_nop 0
	s_nop 0
	s_nop 0
	s_nop 0
	s_nop 0
	s_nop 0
	s_nop 0
	s_nop 0
	s_nop 0
	s_nop 0
	s_nop 0
	s_nop 0
	s_nop 0
	s_nop 0
	s_nop 0
	s_nop 0
	s_nop 0
	s_nop 0
	s_nop 0
	s_nop 0
	s_nop 0
	s_nop 0
	s_nop 0
	s_nop 0
	s_nop 0
	s_nop 0
	s_nop 0
	s_nop 0
	s_nop 0
	s_nop 0
	s_nop 0
	s_nop 0
	s_nop 0
	s_nop 0
	s_nop 0
	s_nop 0
	s_nop 0
	s_nop 0
	s_nop 0
	s_nop 0
	s_nop 0
	s_nop 0
	s_nop 0
	s_nop 0
	s_nop 0
